# speedup vs baseline: 1.0104x; 1.0104x over previous
.LBB1_3:
	s_mov_b32 s29, s16
	v_add_u32_e32 v0, s29, v101
	ds_read_b128 v[94:97], v0 offset:16384
	ds_read_b128 v[102:105], v0 offset:17408
	ds_read_b128 v[106:109], v0 offset:18432
	ds_read_b128 v[110:113], v0 offset:19456
	ds_read_b128 v[114:117], v0 offset:32768
	ds_read_b128 v[118:121], v0 offset:33792
	ds_read_b128 v[122:125], v0 offset:34816
	ds_read_b128 v[126:129], v0 offset:35840
	v_add_u32_e32 v0, s29, v91
	ds_read_b128 v[130:133], v0
	ds_read_b128 v[134:137], v0 offset:1024
	ds_read_b128 v[138:141], v0 offset:2048
	ds_read_b128 v[142:145], v0 offset:3072
	ds_read_b128 v[146:149], v0 offset:4096
	ds_read_b128 v[150:153], v0 offset:5120
	ds_read_b128 v[154:157], v0 offset:6144
	ds_read_b128 v[158:161], v0 offset:7168
	s_lshl_b32 s16, s28, 2
	s_or_b32 s16, s16, s23
	s_lshl_b64 s[30:31], s[16:17], 19
	s_add_u32 s16, s6, s30
	s_addc_u32 s31, s7, s31
	s_lshl_b32 s33, s3, 7
	s_ashr_i32 s35, s33, 31
	s_add_u32 s30, s16, s33
	s_addc_u32 s31, s31, s35
	s_add_u32 s34, s4, s33
	s_addc_u32 s35, s5, s35
	s_add_i32 s16, s19, s27
	s_add_i32 m0, s16, 0x4000
	s_nop 0
	global_load_lds_dwordx4 v84, s[30:31]
	s_add_i32 m0, s16, 0x6000
	s_nop 0
	global_load_lds_dwordx4 v88, s[30:31]
	s_mov_b32 m0, s16
	s_nop 0
	global_load_lds_dwordx4 v82, s[34:35]
	s_waitcnt vmcnt(3)
	s_waitcnt lgkmcnt(0)
	s_barrier
	s_setprio 1
	s_waitcnt lgkmcnt(0)
	v_mfma_f32_16x16x32_f16 v[78:81], v[94:97], v[130:133], v[78:81]
	s_add_u32 s30, s30, 0x40000
	s_addc_u32 s31, s31, 0
	s_add_i32 m0, s16, 0x8000
	v_mfma_f32_16x16x32_f16 v[74:77], v[106:109], v[130:133], v[74:77]
	global_load_lds_dwordx4 v84, s[30:31]
	s_add_i32 m0, s16, 0xa000
	v_mfma_f32_16x16x32_f16 v[66:69], v[94:97], v[138:141], v[66:69]
	global_load_lds_dwordx4 v88, s[30:31]
	s_add_i32 m0, s16, 0x2000
	v_mfma_f32_16x16x32_f16 v[58:61], v[106:109], v[138:141], v[58:61]
	global_load_lds_dwordx4 v86, s[34:35]
	v_mfma_f32_16x16x32_f16 v[78:81], v[102:105], v[134:137], v[78:81]
	v_mfma_f32_16x16x32_f16 v[74:77], v[110:113], v[134:137], v[74:77]
	v_mfma_f32_16x16x32_f16 v[66:69], v[102:105], v[142:145], v[66:69]
	v_mfma_f32_16x16x32_f16 v[58:61], v[110:113], v[142:145], v[58:61]
	v_mfma_f32_16x16x32_f16 v[54:57], v[94:97], v[146:149], v[54:57]
	v_mfma_f32_16x16x32_f16 v[46:49], v[106:109], v[146:149], v[46:49]
	v_mfma_f32_16x16x32_f16 v[34:37], v[94:97], v[154:157], v[34:37]
	v_mfma_f32_16x16x32_f16 v[26:29], v[106:109], v[154:157], v[26:29]
	v_mfma_f32_16x16x32_f16 v[54:57], v[102:105], v[150:153], v[54:57]
	v_mfma_f32_16x16x32_f16 v[46:49], v[110:113], v[150:153], v[46:49]
	v_mfma_f32_16x16x32_f16 v[34:37], v[102:105], v[158:161], v[34:37]
	v_mfma_f32_16x16x32_f16 v[26:29], v[110:113], v[158:161], v[26:29]
	v_mfma_f32_16x16x32_f16 v[70:73], v[114:117], v[130:133], v[70:73]
	v_mfma_f32_16x16x32_f16 v[62:65], v[122:125], v[130:133], v[62:65]
	v_mfma_f32_16x16x32_f16 v[50:53], v[114:117], v[138:141], v[50:53]
	v_mfma_f32_16x16x32_f16 v[42:45], v[122:125], v[138:141], v[42:45]
	v_mfma_f32_16x16x32_f16 v[70:73], v[118:121], v[134:137], v[70:73]
	v_mfma_f32_16x16x32_f16 v[62:65], v[126:129], v[134:137], v[62:65]
	v_mfma_f32_16x16x32_f16 v[50:53], v[118:121], v[142:145], v[50:53]
	v_mfma_f32_16x16x32_f16 v[42:45], v[126:129], v[142:145], v[42:45]
	v_mfma_f32_16x16x32_f16 v[38:41], v[114:117], v[146:149], v[38:41]
	v_mfma_f32_16x16x32_f16 v[30:33], v[122:125], v[146:149], v[30:33]
	s_add_i32 s3, s3, 1
	s_cmp_lt_u32 s28, 2
	s_cselect_b64 s[30:31], -1, 0
	v_mfma_f32_16x16x32_f16 v[22:25], v[114:117], v[154:157], v[22:25]
	s_cmp_eq_u32 s3, 16
	s_cselect_b64 s[34:35], -1, 0
	v_mfma_f32_16x16x32_f16 v[2:5], v[122:125], v[154:157], v[2:5]
	s_and_b64 s[36:37], s[34:35], exec
	s_cselect_b32 s3, 0, s3
	v_mfma_f32_16x16x32_f16 v[38:41], v[118:121], v[150:153], v[38:41]
	s_and_b64 s[30:31], s[34:35], s[30:31]
	s_cmp_lg_u64 s[30:31], 0
	v_mfma_f32_16x16x32_f16 v[30:33], v[126:129], v[150:153], v[30:33]
	s_addc_u32 s28, s28, 0
	s_add_i32 s26, s26, -1
	v_mfma_f32_16x16x32_f16 v[22:25], v[118:121], v[158:161], v[22:25]
	s_mov_b32 s16, s24
	s_mov_b32 s24, s27
	v_mfma_f32_16x16x32_f16 v[2:5], v[126:129], v[158:161], v[2:5]
	s_mov_b32 s27, s29
	s_cmp_lg_u32 s26, 0
	s_setprio 0
	s_barrier
	s_cbranch_scc1 .LBB1_3
	s_lshl_b32 s3, s14, 7
	s_add_i32 s17, s25, s3
	s_ashr_i32 s3, s17, 1
	s_lshr_b32 s14, s17, 5
	s_or_b32 s24, s15, s2
	s_and_b32 s14, s14, 62
	s_and_b32 s27, s3, 0xfffffc00
	v_or_b32_e32 v105, s24, v1
	v_lshlrev_b32_e32 v98, 4, v93
	v_or_b32_e32 v102, 16, v93
	v_or_b32_e32 v103, 32, v93
	v_or_b32_e32 v104, 48, v93
	v_mov_b32_e32 v93, 0
	s_and_b32 s16, s24, 0x340
	v_lshlrev_b32_e32 v95, 6, v105
	s_or_b32 s2, s27, s14
	v_lshlrev_b32_e32 v0, 9, v92
	v_and_b32_e32 v110, 0xc00, v95
	v_mov_b32_e32 v111, v93
	s_or_b32 s14, s2, s16
	v_and_b32_e32 v92, 0x200, v0
	v_lshl_add_u64 v[110:111], s[8:9], 0, v[110:111]
	s_or_b32 s30, s14, 0x80
	s_mov_b32 s3, 0
	v_mov_b32_e32 v99, v93
	v_lshl_add_u64 v[110:111], v[110:111], 0, v[92:93]
	s_mov_b32 s2, 0x3e38aa3b
	v_pk_add_f32 v[72:73], v[12:13], v[72:73]
	v_pk_add_f32 v[70:71], v[10:11], v[70:71]
	v_pk_add_f32 v[64:65], v[8:9], v[64:65]
	v_pk_add_f32 v[62:63], v[6:7], v[62:63]
	s_ashr_i32 s31, s30, 31
	v_lshl_add_u64 v[112:113], v[110:111], 0, v[98:99]
	v_pk_mul_f32 v[72:73], v[72:73], s[2:3] op_sel_hi:[1,0]
	v_pk_mul_f32 v[70:71], v[70:71], s[2:3] op_sel_hi:[1,0]
	v_pk_mul_f32 v[64:65], v[64:65], s[2:3] op_sel_hi:[1,0]
	v_pk_mul_f32 v[62:63], v[62:63], s[2:3] op_sel_hi:[1,0]
	s_lshl_b64 s[30:31], s[30:31], 12
	v_lshlrev_b32_e32 v96, 4, v102
	v_mov_b32_e32 v97, v93
	v_pk_add_f32 v[80:81], v[20:21], v[80:81]
	v_pk_add_f32 v[78:79], v[18:19], v[78:79]
	v_pk_add_f32 v[74:75], v[14:15], v[74:75]
	s_ashr_i32 s15, s14, 31
	v_cvt_pk_f16_f32 v70, v70, v71
	v_cvt_pk_f16_f32 v71, v72, v73
	v_cvt_pk_f16_f32 v72, v62, v63
	v_cvt_pk_f16_f32 v73, v64, v65
	v_lshl_add_u64 v[62:63], v[112:113], 0, s[30:31]
	v_pk_add_f32 v[58:59], v[14:15], v[58:59]
	v_pk_mul_f32 v[80:81], v[80:81], s[2:3] op_sel_hi:[1,0]
	v_pk_mul_f32 v[78:79], v[78:79], s[2:3] op_sel_hi:[1,0]
	v_pk_mul_f32 v[74:75], v[74:75], s[2:3] op_sel_hi:[1,0]
	s_lshl_b64 s[28:29], s[14:15], 12
	global_store_dwordx4 v[62:63], v[70:73], off
	v_pk_add_f32 v[62:63], v[20:21], v[68:69]
	v_pk_add_f32 v[64:65], v[18:19], v[66:67]
	v_lshl_add_u64 v[70:71], v[110:111], 0, v[96:97]
	v_pk_mul_f32 v[58:59], v[58:59], s[2:3] op_sel_hi:[1,0]
	v_pk_add_f32 v[52:53], v[12:13], v[52:53]
	v_pk_add_f32 v[50:51], v[10:11], v[50:51]
	v_pk_add_f32 v[44:45], v[8:9], v[44:45]
	v_pk_add_f32 v[42:43], v[6:7], v[42:43]
	v_lshlrev_b32_e32 v0, 4, v103
	v_cvt_pk_f16_f32 v78, v78, v79
	v_cvt_pk_f16_f32 v79, v80, v81
	v_cvt_pk_f16_f32 v80, v74, v75
	v_lshl_add_u64 v[74:75], v[112:113], 0, s[28:29]
	v_pk_mul_f32 v[66:67], v[62:63], s[2:3] op_sel_hi:[1,0]
	v_pk_mul_f32 v[62:63], v[64:65], s[2:3] op_sel_hi:[1,0]
	v_cvt_pk_f16_f32 v64, v58, v59
	v_lshl_add_u64 v[58:59], v[70:71], 0, s[28:29]
	v_pk_mul_f32 v[52:53], v[52:53], s[2:3] op_sel_hi:[1,0]
	v_pk_mul_f32 v[50:51], v[50:51], s[2:3] op_sel_hi:[1,0]
	v_pk_mul_f32 v[44:45], v[44:45], s[2:3] op_sel_hi:[1,0]
	v_pk_mul_f32 v[42:43], v[42:43], s[2:3] op_sel_hi:[1,0]
	s_or_b32 s28, s14, 1
	s_or_b32 s14, s14, 0x81
	v_and_b32_e32 v106, 0xf0, v0
	v_mov_b32_e32 v107, v93
	v_cvt_pk_f16_f32 v50, v50, v51
	v_cvt_pk_f16_f32 v51, v52, v53
	v_cvt_pk_f16_f32 v52, v42, v43
	v_cvt_pk_f16_f32 v53, v44, v45
	v_lshl_add_u64 v[42:43], v[70:71], 0, s[30:31]
	v_pk_add_f32 v[40:41], v[12:13], v[40:41]
	v_pk_add_f32 v[38:39], v[10:11], v[38:39]
	v_pk_add_f32 v[32:33], v[8:9], v[32:33]
	v_pk_add_f32 v[30:31], v[6:7], v[30:31]
	s_ashr_i32 s15, s14, 31
	v_lshlrev_b32_e32 v94, 4, v104
	global_store_dwordx4 v[42:43], v[50:53], off
	v_pk_mul_f32 v[40:41], v[40:41], s[2:3] op_sel_hi:[1,0]
	v_pk_mul_f32 v[38:39], v[38:39], s[2:3] op_sel_hi:[1,0]
	v_lshl_add_u64 v[50:51], v[110:111], 0, v[106:107]
	v_pk_mul_f32 v[32:33], v[32:33], s[2:3] op_sel_hi:[1,0]
	v_pk_mul_f32 v[30:31], v[30:31], s[2:3] op_sel_hi:[1,0]
	s_lshl_b64 s[14:15], s[14:15], 12
	v_and_b32_e32 v108, 0x1f0, v94
	v_mov_b32_e32 v109, v93
	v_pk_add_f32 v[42:43], v[20:21], v[56:57]
	v_pk_add_f32 v[44:45], v[18:19], v[54:55]
	v_pk_add_f32 v[46:47], v[14:15], v[46:47]
	s_ashr_i32 s29, s28, 31
	v_cvt_pk_f16_f32 v38, v38, v39
	v_cvt_pk_f16_f32 v39, v40, v41
	v_cvt_pk_f16_f32 v40, v30, v31
	v_cvt_pk_f16_f32 v41, v32, v33
	v_lshl_add_u64 v[30:31], v[50:51], 0, s[14:15]
	v_pk_add_f32 v[20:21], v[20:21], v[36:37]
	v_pk_add_f32 v[18:19], v[18:19], v[34:35]
	v_pk_add_f32 v[14:15], v[14:15], v[26:27]
	v_pk_add_f32 v[76:77], v[16:17], v[76:77]
	v_pk_add_f32 v[60:61], v[16:17], v[60:61]
	v_pk_mul_f32 v[52:53], v[42:43], s[2:3] op_sel_hi:[1,0]
	v_pk_mul_f32 v[42:43], v[44:45], s[2:3] op_sel_hi:[1,0]
	v_pk_add_f32 v[44:45], v[16:17], v[48:49]
	s_lshl_b64 s[28:29], s[28:29], 12
	global_store_dwordx4 v[30:31], v[38:41], off
	v_lshl_add_u64 v[30:31], v[110:111], 0, v[108:109]
	v_pk_mul_f32 v[20:21], v[20:21], s[2:3] op_sel_hi:[1,0]
	v_pk_mul_f32 v[18:19], v[18:19], s[2:3] op_sel_hi:[1,0]
	v_pk_add_f32 v[16:17], v[16:17], v[28:29]
	v_pk_mul_f32 v[14:15], v[14:15], s[2:3] op_sel_hi:[1,0]
	v_pk_add_f32 v[12:13], v[12:13], v[24:25]
	v_pk_add_f32 v[10:11], v[10:11], v[22:23]
	v_pk_add_f32 v[4:5], v[8:9], v[4:5]
	v_pk_add_f32 v[2:3], v[6:7], v[2:3]
	v_pk_mul_f32 v[76:77], v[76:77], s[2:3] op_sel_hi:[1,0]
	v_pk_mul_f32 v[60:61], v[60:61], s[2:3] op_sel_hi:[1,0]
	v_pk_mul_f32 v[48:49], v[44:45], s[2:3] op_sel_hi:[1,0]
	v_pk_mul_f32 v[44:45], v[46:47], s[2:3] op_sel_hi:[1,0]
	v_lshl_add_u64 v[46:47], v[50:51], 0, s[28:29]
	v_cvt_pk_f16_f32 v18, v18, v19
	v_cvt_pk_f16_f32 v19, v20, v21
	v_pk_mul_f32 v[16:17], v[16:17], s[2:3] op_sel_hi:[1,0]
	v_cvt_pk_f16_f32 v20, v14, v15
	v_lshl_add_u64 v[14:15], v[30:31], 0, s[28:29]
	v_pk_mul_f32 v[12:13], v[12:13], s[2:3] op_sel_hi:[1,0]
	v_pk_mul_f32 v[10:11], v[10:11], s[2:3] op_sel_hi:[1,0]
	v_pk_mul_f32 v[4:5], v[4:5], s[2:3] op_sel_hi:[1,0]
	v_pk_mul_f32 v[2:3], v[2:3], s[2:3] op_sel_hi:[1,0]
	s_add_u32 s28, s20, s22
	v_cvt_pk_f16_f32 v81, v76, v77
	v_cvt_pk_f16_f32 v62, v62, v63
	v_cvt_pk_f16_f32 v63, v66, v67
	v_cvt_pk_f16_f32 v65, v60, v61
	v_cvt_pk_f16_f32 v42, v42, v43
	v_cvt_pk_f16_f32 v43, v52, v53
	v_cvt_pk_f16_f32 v44, v44, v45
	v_cvt_pk_f16_f32 v45, v48, v49
	v_cvt_pk_f16_f32 v21, v16, v17
	v_cvt_pk_f16_f32 v10, v10, v11
	v_cvt_pk_f16_f32 v11, v12, v13
	v_cvt_pk_f16_f32 v12, v2, v3
	v_cvt_pk_f16_f32 v13, v4, v5
	v_lshl_add_u64 v[2:3], v[30:31], 0, s[14:15]
	s_addc_u32 s29, s21, 0
	v_lshlrev_b32_e32 v92, 2, v1
	global_store_dwordx4 v[74:75], v[78:81], off
	global_store_dwordx4 v[58:59], v[62:65], off
	global_store_dwordx4 v[46:47], v[42:45], off
	global_store_dwordx4 v[14:15], v[18:21], off
	global_store_dwordx4 v[2:3], v[10:13], off
	v_lshl_add_u64 v[2:3], s[28:29], 0, v[92:93]
	s_mov_b64 s[28:29], 0x1000
	v_lshl_add_u64 v[10:11], v[2:3], 0, s[28:29]
	global_load_dwordx4 v[22:25], v[10:11], off
	global_load_dwordx4 v[14:17], v[10:11], off offset:16
	global_load_dwordx4 v[6:9], v[10:11], off offset:512
	global_load_dwordx4 v[2:5], v[10:11], off offset:528
	s_mov_b32 s25, 1
	s_mov_b32 s26, 16
	s_mov_b32 s14, 2
	s_mov_b32 s15, 0x18000
	s_mov_b32 s2, 0xc000
	s_mov_b32 s27, 0
	v_mov_b32_e32 v10, v93
	v_mov_b32_e32 v11, v93
	v_mov_b32_e32 v12, v93
	v_mov_b32_e32 v13, v93
	v_mov_b32_e32 v18, v93
	v_mov_b32_e32 v19, v93
	v_mov_b32_e32 v20, v93
	v_mov_b32_e32 v21, v93
	v_mov_b32_e32 v26, v93
	v_mov_b32_e32 v27, v93
	v_mov_b32_e32 v28, v93
	v_mov_b32_e32 v29, v93
	v_mov_b32_e32 v34, v93
	v_mov_b32_e32 v35, v93
	v_mov_b32_e32 v36, v93
	v_mov_b32_e32 v37, v93
	v_mov_b32_e32 v42, v93
	v_mov_b32_e32 v43, v93
	v_mov_b32_e32 v44, v93
	v_mov_b32_e32 v45, v93
	v_mov_b32_e32 v50, v93
	v_mov_b32_e32 v51, v93
	v_mov_b32_e32 v52, v93
	v_mov_b32_e32 v53, v93
	v_mov_b32_e32 v62, v93
	v_mov_b32_e32 v63, v93
	v_mov_b32_e32 v64, v93
	v_mov_b32_e32 v65, v93
	v_mov_b32_e32 v70, v93
	v_mov_b32_e32 v71, v93
	v_mov_b32_e32 v72, v93
	v_mov_b32_e32 v73, v93
	v_mov_b32_e32 v30, v93
	v_mov_b32_e32 v31, v93
	v_mov_b32_e32 v32, v93
	v_mov_b32_e32 v33, v93
	v_mov_b32_e32 v38, v93
	v_mov_b32_e32 v39, v93
	v_mov_b32_e32 v40, v93
	v_mov_b32_e32 v41, v93
	v_mov_b32_e32 v46, v93
	v_mov_b32_e32 v47, v93
	v_mov_b32_e32 v48, v93
	v_mov_b32_e32 v49, v93
	v_mov_b32_e32 v54, v93
	v_mov_b32_e32 v55, v93
	v_mov_b32_e32 v56, v93
	v_mov_b32_e32 v57, v93
	v_mov_b32_e32 v58, v93
	v_mov_b32_e32 v59, v93
	v_mov_b32_e32 v60, v93
	v_mov_b32_e32 v61, v93
	v_mov_b32_e32 v66, v93
	v_mov_b32_e32 v67, v93
	v_mov_b32_e32 v68, v93
	v_mov_b32_e32 v69, v93
	v_mov_b32_e32 v74, v93
	v_mov_b32_e32 v75, v93
	v_mov_b32_e32 v76, v93
	v_mov_b32_e32 v77, v93
	v_mov_b32_e32 v78, v93
	v_mov_b32_e32 v79, v93
	v_mov_b32_e32 v80, v93
	v_mov_b32_e32 v81, v93
.LBB1_5:
	s_mov_b32 s28, s2
	v_add_u32_e32 v1, s28, v101
	ds_read_b128 v[106:109], v1 offset:16384
	ds_read_b128 v[110:113], v1 offset:17408
	ds_read_b128 v[114:117], v1 offset:18432
	ds_read_b128 v[118:121], v1 offset:19456
	ds_read_b128 v[122:125], v1 offset:32768
	ds_read_b128 v[126:129], v1 offset:33792
	ds_read_b128 v[130:133], v1 offset:34816
	ds_read_b128 v[134:137], v1 offset:35840
	v_add_u32_e32 v1, s28, v91
	ds_read_b128 v[138:141], v1
	ds_read_b128 v[142:145], v1 offset:1024
	ds_read_b128 v[146:149], v1 offset:2048
	ds_read_b128 v[150:153], v1 offset:3072
	ds_read_b128 v[154:157], v1 offset:4096
	ds_read_b128 v[158:161], v1 offset:5120
	ds_read_b128 v[162:165], v1 offset:6144
	ds_read_b128 v[166:169], v1 offset:7168
	s_lshl_b32 s2, s25, 2
	s_or_b32 s2, s2, s23
	s_lshl_b64 s[30:31], s[2:3], 19
	s_add_u32 s2, s6, s30
	s_addc_u32 s29, s7, s31
	s_lshl_b32 s33, s14, 7
	s_ashr_i32 s35, s33, 31
	s_add_u32 s30, s2, s33
	s_addc_u32 s31, s29, s35
	s_add_u32 s34, s4, s33
	s_addc_u32 s35, s5, s35
	s_add_i32 s2, s19, s27
	s_add_i32 m0, s2, 0x4000
	s_nop 0
	global_load_lds_dwordx4 v84, s[30:31]
	s_add_i32 m0, s2, 0x6000
	s_nop 0
	global_load_lds_dwordx4 v88, s[30:31]
	s_mov_b32 m0, s2
	s_nop 0
	global_load_lds_dwordx4 v82, s[34:35]
	s_waitcnt vmcnt(3)
	s_waitcnt lgkmcnt(0)
	s_barrier
	s_setprio 1
	s_waitcnt lgkmcnt(0)
	v_mfma_f32_16x16x32_f16 v[78:81], v[106:109], v[138:141], v[78:81]
	s_add_u32 s30, s30, 0x40000
	s_addc_u32 s31, s31, 0
	s_add_i32 m0, s2, 0x8000
	v_mfma_f32_16x16x32_f16 v[74:77], v[114:117], v[138:141], v[74:77]
	global_load_lds_dwordx4 v84, s[30:31]
	s_add_i32 m0, s2, 0xa000
	v_mfma_f32_16x16x32_f16 v[66:69], v[106:109], v[146:149], v[66:69]
	global_load_lds_dwordx4 v88, s[30:31]
	s_add_i32 m0, s2, 0x2000
	v_mfma_f32_16x16x32_f16 v[58:61], v[114:117], v[146:149], v[58:61]
	global_load_lds_dwordx4 v86, s[34:35]
	v_mfma_f32_16x16x32_f16 v[78:81], v[110:113], v[142:145], v[78:81]
	v_mfma_f32_16x16x32_f16 v[74:77], v[118:121], v[142:145], v[74:77]
	v_mfma_f32_16x16x32_f16 v[66:69], v[110:113], v[150:153], v[66:69]
	v_mfma_f32_16x16x32_f16 v[58:61], v[118:121], v[150:153], v[58:61]
	v_mfma_f32_16x16x32_f16 v[54:57], v[106:109], v[154:157], v[54:57]
	v_mfma_f32_16x16x32_f16 v[46:49], v[114:117], v[154:157], v[46:49]
	v_mfma_f32_16x16x32_f16 v[38:41], v[106:109], v[162:165], v[38:41]
	v_mfma_f32_16x16x32_f16 v[30:33], v[114:117], v[162:165], v[30:33]
	v_mfma_f32_16x16x32_f16 v[54:57], v[110:113], v[158:161], v[54:57]
	v_mfma_f32_16x16x32_f16 v[46:49], v[118:121], v[158:161], v[46:49]
	v_mfma_f32_16x16x32_f16 v[38:41], v[110:113], v[166:169], v[38:41]
	v_mfma_f32_16x16x32_f16 v[30:33], v[118:121], v[166:169], v[30:33]
	v_mfma_f32_16x16x32_f16 v[70:73], v[122:125], v[138:141], v[70:73]
	v_mfma_f32_16x16x32_f16 v[62:65], v[130:133], v[138:141], v[62:65]
	v_mfma_f32_16x16x32_f16 v[50:53], v[122:125], v[146:149], v[50:53]
	v_mfma_f32_16x16x32_f16 v[42:45], v[130:133], v[146:149], v[42:45]
	v_mfma_f32_16x16x32_f16 v[70:73], v[126:129], v[142:145], v[70:73]
	v_mfma_f32_16x16x32_f16 v[62:65], v[134:137], v[142:145], v[62:65]
	v_mfma_f32_16x16x32_f16 v[50:53], v[126:129], v[150:153], v[50:53]
	v_mfma_f32_16x16x32_f16 v[42:45], v[134:137], v[150:153], v[42:45]
	v_mfma_f32_16x16x32_f16 v[34:37], v[122:125], v[154:157], v[34:37]
	v_mfma_f32_16x16x32_f16 v[26:29], v[130:133], v[154:157], v[26:29]
	s_add_i32 s2, s14, 1
	s_cmp_lt_u32 s25, 2
	s_cselect_b64 s[30:31], -1, 0
	v_mfma_f32_16x16x32_f16 v[18:21], v[122:125], v[162:165], v[18:21]
	s_cmp_eq_u32 s2, 16
	s_cselect_b64 s[34:35], -1, 0
	v_mfma_f32_16x16x32_f16 v[10:13], v[130:133], v[162:165], v[10:13]
	s_and_b64 s[36:37], s[34:35], exec
	s_cselect_b32 s14, 0, s2
	v_mfma_f32_16x16x32_f16 v[34:37], v[126:129], v[158:161], v[34:37]
	s_and_b64 s[30:31], s[34:35], s[30:31]
	s_cmp_lg_u64 s[30:31], 0
	v_mfma_f32_16x16x32_f16 v[26:29], v[134:137], v[158:161], v[26:29]
	s_addc_u32 s25, s25, 0
	s_add_i32 s26, s26, -1
	v_mfma_f32_16x16x32_f16 v[18:21], v[126:129], v[166:169], v[18:21]
	s_mov_b32 s2, s15
	s_mov_b32 s15, s27
	v_mfma_f32_16x16x32_f16 v[10:13], v[134:137], v[166:169], v[10:13]
	s_mov_b32 s27, s28
	s_cmp_lg_u32 s26, 0
	s_setprio 0
	s_barrier
	s_cbranch_scc1 .LBB1_5
	s_ashr_i32 s2, s17, 7
	s_and_b32 s3, s2, -16
	s_or_b32 s2, s3, 2
	s_sub_u32 s14, s10, s8
	s_subb_u32 s11, s11, s9
	s_bfe_u32 s6, s17, 0x50006
	s_add_u32 s14, s8, s14
	s_addc_u32 s15, s9, s11
	s_lshr_b32 s11, s24, 6
	s_or_b32 s17, s11, s3
	s_lshl_b32 s17, s17, 8
	s_lshl_b32 s23, s6, 3
	v_bfe_u32 v93, v105, 3, 3
	v_pk_add_f32 v[80:81], v[24:25], v[80:81]
	v_pk_add_f32 v[78:79], v[22:23], v[78:79]
	v_pk_add_f32 v[74:75], v[14:15], v[74:75]
	s_or_b32 s17, s17, s23
	s_or_b32 s11, s2, s11
	v_cvt_pk_f16_f32 v78, v78, v79
	v_cvt_pk_f16_f32 v79, v80, v81
	v_cvt_pk_f16_f32 v80, v74, v75
	v_or_b32_e32 v74, s17, v93
	s_lshl_b32 s11, s11, 8
	v_ashrrev_i32_e32 v75, 31, v74
	v_pk_add_f32 v[72:73], v[8:9], v[72:73]
	v_pk_add_f32 v[70:71], v[6:7], v[70:71]
	v_pk_add_f32 v[62:63], v[2:3], v[62:63]
	s_or_b32 s11, s11, s23
	v_lshlrev_b64 v[74:75], 10, v[74:75]
	v_cvt_pk_f16_f32 v70, v70, v71
	v_cvt_pk_f16_f32 v71, v72, v73
	v_cvt_pk_f16_f32 v72, v62, v63
	v_or_b32_e32 v62, s11, v93
	v_pk_add_f32 v[76:77], v[16:17], v[76:77]
	v_lshl_add_u64 v[74:75], s[14:15], 0, v[74:75]
	v_ashrrev_i32_e32 v63, 31, v62
	v_cvt_pk_f16_f32 v81, v76, v77
	v_lshl_add_u64 v[76:77], v[74:75], 0, v[98:99]
	v_lshlrev_b64 v[62:63], 10, v[62:63]
	global_store_dwordx4 v[76:77], v[78:81], off
	v_pk_add_f32 v[64:65], v[4:5], v[64:65]
	v_lshl_add_u64 v[76:77], s[14:15], 0, v[62:63]
	v_cvt_pk_f16_f32 v73, v64, v65
	v_lshl_add_u64 v[62:63], v[76:77], 0, v[98:99]
	global_store_dwordx4 v[62:63], v[70:73], off
	v_pk_add_f32 v[64:65], v[24:25], v[68:69]
	v_pk_add_f32 v[62:63], v[22:23], v[66:67]
	v_pk_add_f32 v[60:61], v[16:17], v[60:61]
	v_pk_add_f32 v[58:59], v[14:15], v[58:59]
	v_pk_add_f32 v[52:53], v[8:9], v[52:53]
	v_pk_add_f32 v[50:51], v[6:7], v[50:51]
	v_pk_add_f32 v[44:45], v[4:5], v[44:45]
	v_pk_add_f32 v[42:43], v[2:3], v[42:43]
	v_cvt_pk_f16_f32 v62, v62, v63
	v_cvt_pk_f16_f32 v63, v64, v65
	v_cvt_pk_f16_f32 v64, v58, v59
	v_cvt_pk_f16_f32 v65, v60, v61
	v_lshl_add_u64 v[58:59], v[74:75], 0, v[96:97]
	v_cvt_pk_f16_f32 v50, v50, v51
	v_cvt_pk_f16_f32 v51, v52, v53
	v_cvt_pk_f16_f32 v52, v42, v43
	v_cvt_pk_f16_f32 v53, v44, v45
	v_lshl_add_u64 v[42:43], v[76:77], 0, v[96:97]
	v_mov_b32_e32 v1, 0
	global_store_dwordx4 v[58:59], v[62:65], off
	global_store_dwordx4 v[42:43], v[50:53], off
	v_pk_add_f32 v[44:45], v[24:25], v[56:57]
	v_pk_add_f32 v[42:43], v[22:23], v[54:55]
	v_mov_b32_e32 v95, v1
	v_cvt_pk_f16_f32 v42, v42, v43
	v_cvt_pk_f16_f32 v43, v44, v45
	v_pk_add_f32 v[48:49], v[16:17], v[48:49]
	v_pk_add_f32 v[44:45], v[14:15], v[46:47]
	v_pk_add_f32 v[36:37], v[8:9], v[36:37]
	v_pk_add_f32 v[34:35], v[6:7], v[34:35]
	v_pk_add_f32 v[28:29], v[4:5], v[28:29]
	v_pk_add_f32 v[26:27], v[2:3], v[26:27]
	v_pk_add_f32 v[24:25], v[24:25], v[40:41]
	v_pk_add_f32 v[22:23], v[22:23], v[38:39]
	v_pk_add_f32 v[16:17], v[16:17], v[32:33]
	v_pk_add_f32 v[14:15], v[14:15], v[30:31]
	v_pk_add_f32 v[8:9], v[8:9], v[20:21]
	v_pk_add_f32 v[6:7], v[6:7], v[18:19]
	v_pk_add_f32 v[4:5], v[4:5], v[12:13]
	v_pk_add_f32 v[2:3], v[2:3], v[10:11]
	s_add_u32 s14, s20, s22
	v_cvt_pk_f16_f32 v44, v44, v45
	v_cvt_pk_f16_f32 v45, v48, v49
	v_lshl_add_u64 v[46:47], v[74:75], 0, v[0:1]
	v_cvt_pk_f16_f32 v34, v34, v35
	v_cvt_pk_f16_f32 v35, v36, v37
	v_cvt_pk_f16_f32 v36, v26, v27
	v_cvt_pk_f16_f32 v37, v28, v29
	v_lshl_add_u64 v[26:27], v[76:77], 0, v[0:1]
	v_cvt_pk_f16_f32 v22, v22, v23
	v_cvt_pk_f16_f32 v23, v24, v25
	v_cvt_pk_f16_f32 v24, v14, v15
	v_cvt_pk_f16_f32 v25, v16, v17
	v_lshl_add_u64 v[14:15], v[74:75], 0, v[94:95]
	v_cvt_pk_f16_f32 v6, v6, v7
	v_cvt_pk_f16_f32 v7, v8, v9
	v_cvt_pk_f16_f32 v8, v2, v3
	v_cvt_pk_f16_f32 v9, v4, v5
	v_lshl_add_u64 v[2:3], v[76:77], 0, v[94:95]
	s_addc_u32 s15, s21, 0
	v_mov_b32_e32 v93, v1
	global_store_dwordx4 v[46:47], v[42:45], off
	global_store_dwordx4 v[26:27], v[34:37], off
	global_store_dwordx4 v[14:15], v[22:25], off
	global_store_dwordx4 v[2:3], v[6:9], off
	v_lshl_add_u64 v[2:3], s[14:15], 0, v[92:93]
	s_mov_b64 s[14:15], 0x2000
	v_lshl_add_u64 v[2:3], v[2:3], 0, s[14:15]
	global_load_dwordx4 v[20:23], v[2:3], off
	global_load_dwordx4 v[12:15], v[2:3], off offset:16
	global_load_dwordx4 v[8:11], v[2:3], off offset:512
	global_load_dwordx4 v[4:7], v[2:3], off offset:528
	s_add_u32 s11, s12, 0x400000
	s_mov_b32 s7, 2
	v_and_b32_e32 v106, 56, v105
	s_mov_b32 s10, 0
	s_addc_u32 s12, s13, 0
	s_mov_b32 s14, 0xc000
	s_mov_b32 s17, 0x18000
	s_mov_b32 s13, 16
	v_mov_b32_e32 v0, v1
	v_mov_b32_e32 v2, v1
	v_mov_b32_e32 v3, v1
	v_mov_b32_e32 v16, v1
	v_mov_b32_e32 v17, v1
	v_mov_b32_e32 v18, v1
	v_mov_b32_e32 v19, v1
	v_mov_b32_e32 v24, v1
	v_mov_b32_e32 v25, v1
	v_mov_b32_e32 v26, v1
	v_mov_b32_e32 v27, v1
	v_mov_b32_e32 v32, v1
	v_mov_b32_e32 v33, v1
	v_mov_b32_e32 v34, v1
	v_mov_b32_e32 v35, v1
	v_mov_b32_e32 v40, v1
	v_mov_b32_e32 v41, v1
	v_mov_b32_e32 v42, v1
	v_mov_b32_e32 v43, v1
	v_mov_b32_e32 v48, v1
	v_mov_b32_e32 v49, v1
	v_mov_b32_e32 v50, v1
	v_mov_b32_e32 v51, v1
	v_mov_b32_e32 v60, v1
	v_mov_b32_e32 v61, v1
	v_mov_b32_e32 v62, v1
	v_mov_b32_e32 v63, v1
	v_mov_b32_e32 v68, v1
	v_mov_b32_e32 v69, v1
	v_mov_b32_e32 v70, v1
	v_mov_b32_e32 v71, v1
	v_mov_b32_e32 v28, v1
	v_mov_b32_e32 v29, v1
	v_mov_b32_e32 v30, v1
	v_mov_b32_e32 v31, v1
	v_mov_b32_e32 v36, v1
	v_mov_b32_e32 v37, v1
	v_mov_b32_e32 v38, v1
	v_mov_b32_e32 v39, v1
	v_mov_b32_e32 v44, v1
	v_mov_b32_e32 v45, v1
	v_mov_b32_e32 v46, v1
	v_mov_b32_e32 v47, v1
	v_mov_b32_e32 v52, v1
	v_mov_b32_e32 v53, v1
	v_mov_b32_e32 v54, v1
	v_mov_b32_e32 v55, v1
	v_mov_b32_e32 v56, v1
	v_mov_b32_e32 v57, v1
	v_mov_b32_e32 v58, v1
	v_mov_b32_e32 v59, v1
	v_mov_b32_e32 v64, v1
	v_mov_b32_e32 v65, v1
	v_mov_b32_e32 v66, v1
	v_mov_b32_e32 v67, v1
	v_mov_b32_e32 v72, v1
	v_mov_b32_e32 v73, v1
	v_mov_b32_e32 v74, v1
	v_mov_b32_e32 v75, v1
	v_mov_b32_e32 v76, v1
	v_mov_b32_e32 v77, v1
	v_mov_b32_e32 v78, v1
	v_mov_b32_e32 v79, v1
